# baseline (speedup 1.0000x reference)
.LBB1_4:
	s_setprio 2
	s_load_dwordx2 s[0:1], s[0:1], 0x0
	v_add_u32_e32 v2, 0xffffff00, v0
	v_ashrrev_i32_e32 v20, 4, v2
	v_add_u32_e32 v2, s12, v20
	v_ashrrev_i32_e32 v3, 31, v2
	v_lshlrev_b64 v[2:3], 12, v[2:3]
	s_lshl_b32 s2, s3, 6
	s_waitcnt lgkmcnt(0)
	v_lshl_add_u64 v[2:3], s[0:1], 0, v[2:3]
	v_lshlrev_b32_e32 v4, 4, v1
	v_mov_b32_e32 v5, 0
	s_and_b32 s6, s2, 0x3c0
	s_mov_b32 s1, 0
	v_lshl_add_u64 v[2:3], v[2:3], 0, v[4:5]
	s_lshl_b32 s0, s6, 2
	v_lshl_add_u64 v[16:17], v[2:3], 0, s[0:1]
	s_mov_b32 s3, 0x10000
	v_add_co_u32_e32 v12, vcc, s3, v16
	s_mov_b32 s4, 0x20000
	s_nop 0
	v_addc_co_u32_e32 v13, vcc, 0, v17, vcc
	global_load_dwordx4 v[4:7], v[16:17], off sc0 sc1 nt
	global_load_dwordx4 v[8:11], v[12:13], off sc0 sc1 nt
	v_add_co_u32_e32 v12, vcc, s4, v16
	s_mov_b32 s5, 0x30000
	s_nop 0
	v_addc_co_u32_e32 v13, vcc, 0, v17, vcc
	s_add_i32 s0, s2, 64
	global_load_dwordx4 v[12:15], v[12:13], off sc0 sc1 nt
	v_add_co_u32_e32 v16, vcc, s5, v16
	s_and_b32 s0, s0, 0x3c0
	s_nop 0
	v_addc_co_u32_e32 v17, vcc, 0, v17, vcc
	s_lshl_b32 s0, s0, 2
	global_load_dwordx4 v[16:19], v[16:17], off sc0 sc1 nt
	v_lshl_add_u64 v[28:29], v[2:3], 0, s[0:1]
	v_lshrrev_b32_e32 v1, 1, v1
	v_lshrrev_b32_e32 v21, 5, v0
	v_lshlrev_b32_e32 v0, 3, v0
	v_add_co_u32_e32 v30, vcc, s3, v28
	v_bitop3_b32 v1, v1, v21, 7 bitop3:0x78
	v_and_b32_e32 v0, 8, v0
	v_addc_co_u32_e32 v31, vcc, 0, v29, vcc
	v_lshl_or_b32 v0, v1, 4, v0
	v_add_co_u32_e32 v36, vcc, s4, v28
	v_lshl_or_b32 v0, v20, 7, v0
	global_load_dwordx4 v[20:23], v[28:29], off sc0 sc1 nt
	global_load_dwordx4 v[24:27], v[30:31], off sc0 sc1 nt
	v_addc_co_u32_e32 v37, vcc, 0, v29, vcc
	s_add_i32 s0, s2, 0x80
	v_add_co_u32_e32 v38, vcc, s5, v28
	s_and_b32 s0, s0, 0x3c0
	s_nop 0
	v_addc_co_u32_e32 v39, vcc, 0, v29, vcc
	global_load_dwordx4 v[28:31], v[36:37], off sc0 sc1 nt
	global_load_dwordx4 v[32:35], v[38:39], off sc0 sc1 nt
	s_lshl_b32 s0, s0, 2
	v_lshl_add_u64 v[44:45], v[2:3], 0, s[0:1]
	v_add_co_u32_e32 v46, vcc, s3, v44
	s_add_i32 s0, s2, 0xc0
	s_nop 0
	v_addc_co_u32_e32 v47, vcc, 0, v45, vcc
	v_add_co_u32_e32 v52, vcc, s4, v44
	global_load_dwordx4 v[36:39], v[44:45], off sc0 sc1 nt
	global_load_dwordx4 v[40:43], v[46:47], off sc0 sc1 nt
	v_addc_co_u32_e32 v53, vcc, 0, v45, vcc
	v_add_co_u32_e32 v54, vcc, s5, v44
	s_and_b32 s0, s0, 0x3c0
	s_nop 0
	v_addc_co_u32_e32 v55, vcc, 0, v45, vcc
	global_load_dwordx4 v[44:47], v[52:53], off sc0 sc1 nt
	global_load_dwordx4 v[48:51], v[54:55], off sc0 sc1 nt
	s_lshl_b32 s0, s0, 2
	v_lshl_add_u64 v[60:61], v[2:3], 0, s[0:1]
	v_add_co_u32_e32 v62, vcc, s3, v60
	s_add_i32 s0, s2, 0x100
	s_nop 0
	v_addc_co_u32_e32 v63, vcc, 0, v61, vcc
	v_add_co_u32_e32 v68, vcc, s4, v60
	global_load_dwordx4 v[52:55], v[60:61], off sc0 sc1 nt
	global_load_dwordx4 v[56:59], v[62:63], off sc0 sc1 nt
	v_addc_co_u32_e32 v69, vcc, 0, v61, vcc
	v_add_co_u32_e32 v70, vcc, s5, v60
	s_and_b32 s0, s0, 0x3c0
	s_nop 0
	v_addc_co_u32_e32 v71, vcc, 0, v61, vcc
	global_load_dwordx4 v[60:63], v[68:69], off sc0 sc1 nt
	global_load_dwordx4 v[64:67], v[70:71], off sc0 sc1 nt
	s_lshl_b32 s0, s0, 2
	v_add_u32_e32 v1, 0x10000, v0
	s_waitcnt vmcnt(15)
	v_cvt_pk_f16_f32 v7, v6, v7
	v_cvt_pk_f16_f32 v6, v4, v5
	s_waitcnt vmcnt(14)
	v_cvt_pk_f16_f32 v5, v10, v11
	v_cvt_pk_f16_f32 v4, v8, v9
	ds_write2st64_b64 v0, v[6:7], v[4:5] offset1:4
	s_waitcnt vmcnt(13)
	v_cvt_pk_f16_f32 v4, v12, v13
	v_lshl_add_u64 v[12:13], v[2:3], 0, s[0:1]
	v_cvt_pk_f16_f32 v5, v14, v15
	v_add_co_u32_e32 v14, vcc, s3, v12
	s_add_i32 s0, s2, 0x140
	s_nop 0
	v_addc_co_u32_e32 v15, vcc, 0, v13, vcc
	s_waitcnt vmcnt(12)
	v_cvt_pk_f16_f32 v7, v18, v19
	v_cvt_pk_f16_f32 v6, v16, v17
	ds_write2st64_b64 v0, v[4:5], v[6:7] offset0:8 offset1:12
	v_add_co_u32_e32 v68, vcc, s4, v12
	global_load_dwordx4 v[4:7], v[12:13], off sc0 sc1 nt
	global_load_dwordx4 v[8:11], v[14:15], off sc0 sc1 nt
	v_addc_co_u32_e32 v69, vcc, 0, v13, vcc
	v_add_co_u32_e32 v70, vcc, s5, v12
	s_and_b32 s0, s0, 0x3c0
	s_nop 0
	v_addc_co_u32_e32 v71, vcc, 0, v13, vcc
	global_load_dwordx4 v[12:15], v[68:69], off sc0 sc1 nt
	global_load_dwordx4 v[16:19], v[70:71], off sc0 sc1 nt
	s_waitcnt vmcnt(15)
	v_cvt_pk_f16_f32 v23, v22, v23
	v_cvt_pk_f16_f32 v22, v20, v21
	s_waitcnt vmcnt(14)
	v_cvt_pk_f16_f32 v21, v26, v27
	v_cvt_pk_f16_f32 v20, v24, v25
	s_lshl_b32 s0, s0, 2
	s_waitcnt lgkmcnt(0)
	v_add_u32_e32 v171, 1, v171
	ds_write_b32 v169, v171
	ds_write2st64_b64 v0, v[22:23], v[20:21] offset0:16 offset1:20
	s_waitcnt vmcnt(13)
	v_cvt_pk_f16_f32 v20, v28, v29
	v_lshl_add_u64 v[28:29], v[2:3], 0, s[0:1]
	v_cvt_pk_f16_f32 v21, v30, v31
	v_add_co_u32_e32 v30, vcc, s3, v28
	s_waitcnt vmcnt(12)
	v_cvt_pk_f16_f32 v23, v34, v35
	v_cvt_pk_f16_f32 v22, v32, v33
	v_addc_co_u32_e32 v31, vcc, 0, v29, vcc
	ds_write2st64_b64 v0, v[20:21], v[22:23] offset0:24 offset1:28
	v_add_co_u32_e32 v68, vcc, s4, v28
	global_load_dwordx4 v[20:23], v[28:29], off sc0 sc1 nt
	global_load_dwordx4 v[24:27], v[30:31], off sc0 sc1 nt
	v_addc_co_u32_e32 v69, vcc, 0, v29, vcc
	s_add_i32 s0, s2, 0x180
	v_add_co_u32_e32 v70, vcc, s5, v28
	s_and_b32 s0, s0, 0x3c0
	s_nop 0
	v_addc_co_u32_e32 v71, vcc, 0, v29, vcc
	global_load_dwordx4 v[28:31], v[68:69], off sc0 sc1 nt
	global_load_dwordx4 v[32:35], v[70:71], off sc0 sc1 nt
	s_waitcnt vmcnt(15)
	v_cvt_pk_f16_f32 v39, v38, v39
	v_cvt_pk_f16_f32 v38, v36, v37
	s_waitcnt vmcnt(14)
	v_cvt_pk_f16_f32 v37, v42, v43
	v_cvt_pk_f16_f32 v36, v40, v41
	s_lshl_b32 s0, s0, 2
	s_waitcnt lgkmcnt(0)
	v_add_u32_e32 v171, 1, v171
	ds_write_b32 v169, v171
	ds_write2st64_b64 v0, v[38:39], v[36:37] offset0:32 offset1:36
	s_waitcnt vmcnt(13)
	v_cvt_pk_f16_f32 v36, v44, v45
	v_lshl_add_u64 v[44:45], v[2:3], 0, s[0:1]
	v_cvt_pk_f16_f32 v37, v46, v47
	v_add_co_u32_e32 v46, vcc, s3, v44
	s_waitcnt vmcnt(12)
	v_cvt_pk_f16_f32 v39, v50, v51
	v_cvt_pk_f16_f32 v38, v48, v49
	v_addc_co_u32_e32 v47, vcc, 0, v45, vcc
	ds_write2st64_b64 v0, v[36:37], v[38:39] offset0:40 offset1:44
	v_add_co_u32_e32 v68, vcc, s4, v44
	global_load_dwordx4 v[36:39], v[44:45], off sc0 sc1 nt
	global_load_dwordx4 v[40:43], v[46:47], off sc0 sc1 nt
	v_addc_co_u32_e32 v69, vcc, 0, v45, vcc
	v_add_co_u32_e32 v70, vcc, s5, v44
	s_add_i32 s0, s2, 0x1c0
	s_nop 0
	v_addc_co_u32_e32 v71, vcc, 0, v45, vcc
	global_load_dwordx4 v[44:47], v[68:69], off sc0 sc1 nt
	global_load_dwordx4 v[48:51], v[70:71], off sc0 sc1 nt
	s_and_b32 s0, s0, 0x3c0
	s_waitcnt vmcnt(15)
	v_cvt_pk_f16_f32 v55, v54, v55
	v_cvt_pk_f16_f32 v54, v52, v53
	s_waitcnt vmcnt(14)
	v_cvt_pk_f16_f32 v53, v58, v59
	v_cvt_pk_f16_f32 v52, v56, v57
	s_lshl_b32 s0, s0, 2
	s_waitcnt lgkmcnt(0)
	v_add_u32_e32 v171, 1, v171
	ds_write_b32 v169, v171
	ds_write2st64_b64 v0, v[54:55], v[52:53] offset0:48 offset1:52
	s_waitcnt vmcnt(13)
	v_cvt_pk_f16_f32 v52, v60, v61
	v_lshl_add_u64 v[60:61], v[2:3], 0, s[0:1]
	v_cvt_pk_f16_f32 v53, v62, v63
	v_add_co_u32_e32 v62, vcc, s3, v60
	s_waitcnt vmcnt(12)
	v_cvt_pk_f16_f32 v55, v66, v67
	v_addc_co_u32_e32 v63, vcc, 0, v61, vcc
	v_cvt_pk_f16_f32 v54, v64, v65
	v_add_co_u32_e32 v68, vcc, s4, v60
	ds_write2st64_b64 v0, v[52:53], v[54:55] offset0:56 offset1:60
	s_nop 0
	v_addc_co_u32_e32 v69, vcc, 0, v61, vcc
	global_load_dwordx4 v[52:55], v[60:61], off sc0 sc1 nt
	global_load_dwordx4 v[56:59], v[62:63], off sc0 sc1 nt
	v_add_co_u32_e32 v70, vcc, s5, v60
	s_xor_b32 s0, s6, 0x200
	s_nop 0
	v_addc_co_u32_e32 v71, vcc, 0, v61, vcc
	global_load_dwordx4 v[60:63], v[68:69], off sc0 sc1 nt
	global_load_dwordx4 v[64:67], v[70:71], off sc0 sc1 nt
	s_waitcnt vmcnt(15)
	v_cvt_pk_f16_f32 v7, v6, v7
	v_cvt_pk_f16_f32 v6, v4, v5
	s_waitcnt vmcnt(14)
	v_cvt_pk_f16_f32 v5, v10, v11
	v_cvt_pk_f16_f32 v4, v8, v9
	s_lshl_b32 s0, s0, 2
	s_waitcnt lgkmcnt(0)
	v_add_u32_e32 v171, 1, v171
	ds_write_b32 v169, v171
	ds_write2st64_b64 v0, v[6:7], v[4:5] offset0:64 offset1:68
	s_waitcnt vmcnt(13)
	v_cvt_pk_f16_f32 v4, v12, v13
	v_lshl_add_u64 v[12:13], v[2:3], 0, s[0:1]
	v_cvt_pk_f16_f32 v5, v14, v15
	v_add_co_u32_e32 v14, vcc, s3, v12
	s_waitcnt vmcnt(12)
	v_cvt_pk_f16_f32 v7, v18, v19
	v_cvt_pk_f16_f32 v6, v16, v17
	v_addc_co_u32_e32 v15, vcc, 0, v13, vcc
	ds_write2st64_b64 v0, v[4:5], v[6:7] offset0:72 offset1:76
	v_add_co_u32_e32 v68, vcc, s4, v12
	global_load_dwordx4 v[4:7], v[12:13], off sc0 sc1 nt
	global_load_dwordx4 v[8:11], v[14:15], off sc0 sc1 nt
	v_addc_co_u32_e32 v69, vcc, 0, v13, vcc
	s_add_i32 s0, s2, 0x240
	v_add_co_u32_e32 v70, vcc, s5, v12
	s_and_b32 s0, s0, 0x3c0
	s_nop 0
	v_addc_co_u32_e32 v71, vcc, 0, v13, vcc
	global_load_dwordx4 v[12:15], v[68:69], off sc0 sc1 nt
	global_load_dwordx4 v[16:19], v[70:71], off sc0 sc1 nt
	s_waitcnt vmcnt(15)
	v_cvt_pk_f16_f32 v23, v22, v23
	v_cvt_pk_f16_f32 v22, v20, v21
	s_waitcnt vmcnt(14)
	v_cvt_pk_f16_f32 v21, v26, v27
	v_cvt_pk_f16_f32 v20, v24, v25
	s_lshl_b32 s0, s0, 2
	s_waitcnt lgkmcnt(0)
	v_add_u32_e32 v171, 1, v171
	ds_write_b32 v169, v171
	ds_write2st64_b64 v0, v[22:23], v[20:21] offset0:80 offset1:84
	s_waitcnt vmcnt(13)
	v_cvt_pk_f16_f32 v20, v28, v29
	v_lshl_add_u64 v[28:29], v[2:3], 0, s[0:1]
	v_cvt_pk_f16_f32 v21, v30, v31
	v_add_co_u32_e32 v30, vcc, s3, v28
	s_waitcnt vmcnt(12)
	v_cvt_pk_f16_f32 v23, v34, v35
	v_cvt_pk_f16_f32 v22, v32, v33
	v_addc_co_u32_e32 v31, vcc, 0, v29, vcc
	ds_write2st64_b64 v0, v[20:21], v[22:23] offset0:88 offset1:92
	v_add_co_u32_e32 v68, vcc, s4, v28
	global_load_dwordx4 v[20:23], v[28:29], off sc0 sc1 nt
	global_load_dwordx4 v[24:27], v[30:31], off sc0 sc1 nt
	v_addc_co_u32_e32 v69, vcc, 0, v29, vcc
	s_add_i32 s0, s2, 0x280
	v_add_co_u32_e32 v70, vcc, s5, v28
	s_and_b32 s0, s0, 0x3c0
	s_nop 0
	v_addc_co_u32_e32 v71, vcc, 0, v29, vcc
	global_load_dwordx4 v[28:31], v[68:69], off sc0 sc1 nt
	global_load_dwordx4 v[32:35], v[70:71], off sc0 sc1 nt
	s_waitcnt vmcnt(15)
	v_cvt_pk_f16_f32 v39, v38, v39
	v_cvt_pk_f16_f32 v38, v36, v37
	s_waitcnt vmcnt(14)
	v_cvt_pk_f16_f32 v37, v42, v43
	v_cvt_pk_f16_f32 v36, v40, v41
	s_lshl_b32 s0, s0, 2
	s_waitcnt lgkmcnt(0)
	v_add_u32_e32 v171, 1, v171
	ds_write_b32 v169, v171
	ds_write2st64_b64 v0, v[38:39], v[36:37] offset0:96 offset1:100
	s_waitcnt vmcnt(13)
	v_cvt_pk_f16_f32 v36, v44, v45
	v_lshl_add_u64 v[44:45], v[2:3], 0, s[0:1]
	v_cvt_pk_f16_f32 v37, v46, v47
	v_add_co_u32_e32 v46, vcc, s3, v44
	s_waitcnt vmcnt(12)
	v_cvt_pk_f16_f32 v39, v50, v51
	v_cvt_pk_f16_f32 v38, v48, v49
	v_addc_co_u32_e32 v47, vcc, 0, v45, vcc
	ds_write2st64_b64 v0, v[36:37], v[38:39] offset0:104 offset1:108
	v_add_co_u32_e32 v68, vcc, s4, v44
	global_load_dwordx4 v[36:39], v[44:45], off sc0 sc1 nt
	global_load_dwordx4 v[40:43], v[46:47], off sc0 sc1 nt
	v_addc_co_u32_e32 v69, vcc, 0, v45, vcc
	v_add_co_u32_e32 v70, vcc, s5, v44
	s_add_i32 s0, s2, 0x2c0
	s_nop 0
	v_addc_co_u32_e32 v71, vcc, 0, v45, vcc
	global_load_dwordx4 v[44:47], v[68:69], off sc0 sc1 nt
	global_load_dwordx4 v[48:51], v[70:71], off sc0 sc1 nt
	s_and_b32 s0, s0, 0x3c0
	s_waitcnt vmcnt(15)
	v_cvt_pk_f16_f32 v55, v54, v55
	v_cvt_pk_f16_f32 v54, v52, v53
	s_waitcnt vmcnt(14)
	v_cvt_pk_f16_f32 v53, v58, v59
	v_cvt_pk_f16_f32 v52, v56, v57
	s_lshl_b32 s0, s0, 2
	s_waitcnt lgkmcnt(0)
	v_add_u32_e32 v171, 1, v171
	ds_write_b32 v169, v171
	ds_write2st64_b64 v0, v[54:55], v[52:53] offset0:112 offset1:116
	s_waitcnt vmcnt(13)
	v_cvt_pk_f16_f32 v53, v62, v63
	v_cvt_pk_f16_f32 v52, v60, v61
	s_waitcnt vmcnt(12)
	v_cvt_pk_f16_f32 v55, v66, v67
	v_cvt_pk_f16_f32 v54, v64, v65
	v_lshl_add_u64 v[60:61], v[2:3], 0, s[0:1]
	ds_write2st64_b64 v0, v[52:53], v[54:55] offset0:120 offset1:124
	v_add_co_u32_e32 v62, vcc, s3, v60
	s_add_i32 s0, s2, 0x300
	s_nop 0
	v_addc_co_u32_e32 v63, vcc, 0, v61, vcc
	global_load_dwordx4 v[52:55], v[60:61], off sc0 sc1 nt
	global_load_dwordx4 v[56:59], v[62:63], off sc0 sc1 nt
	v_add_co_u32_e32 v68, vcc, s4, v60
	s_waitcnt vmcnt(13)
	v_cvt_pk_f16_f32 v7, v6, v7
	v_addc_co_u32_e32 v69, vcc, 0, v61, vcc
	v_add_co_u32_e32 v70, vcc, s5, v60
	v_cvt_pk_f16_f32 v6, v4, v5
	s_and_b32 s0, s0, 0x3c0
	v_addc_co_u32_e32 v71, vcc, 0, v61, vcc
	global_load_dwordx4 v[60:63], v[68:69], off sc0 sc1 nt
	global_load_dwordx4 v[64:67], v[70:71], off sc0 sc1 nt
	s_waitcnt lgkmcnt(0)
	v_add_u32_e32 v171, 1, v171
	ds_write_b32 v169, v171
	ds_write_b64 v1, v[6:7]
	s_waitcnt vmcnt(14)
	v_cvt_pk_f16_f32 v5, v10, v11
	v_cvt_pk_f16_f32 v4, v8, v9
	v_add_u32_e32 v1, 0x10800, v0
	s_lshl_b32 s0, s0, 2
	ds_write_b64 v1, v[4:5]
	s_waitcnt vmcnt(13)
	v_cvt_pk_f16_f32 v4, v12, v13
	v_lshl_add_u64 v[12:13], v[2:3], 0, s[0:1]
	v_cvt_pk_f16_f32 v5, v14, v15
	v_add_co_u32_e32 v14, vcc, s3, v12
	v_add_u32_e32 v1, 0x11000, v0
	s_nop 0
	v_addc_co_u32_e32 v15, vcc, 0, v13, vcc
	v_add_co_u32_e32 v68, vcc, s4, v12
	ds_write_b64 v1, v[4:5]
	s_waitcnt vmcnt(12)
	v_cvt_pk_f16_f32 v5, v18, v19
	v_cvt_pk_f16_f32 v4, v16, v17
	v_add_u32_e32 v1, 0x11800, v0
	v_addc_co_u32_e32 v69, vcc, 0, v13, vcc
	s_add_i32 s0, s2, 0x340
	ds_write_b64 v1, v[4:5]
	v_add_co_u32_e32 v70, vcc, s5, v12
	s_waitcnt vmcnt(11)
	v_cvt_pk_f16_f32 v23, v22, v23
	v_cvt_pk_f16_f32 v22, v20, v21
	v_add_u32_e32 v1, 0x12000, v0
	s_and_b32 s0, s0, 0x3c0
	global_load_dwordx4 v[4:7], v[12:13], off sc0 sc1 nt
	global_load_dwordx4 v[8:11], v[14:15], off sc0 sc1 nt
	v_addc_co_u32_e32 v71, vcc, 0, v13, vcc
	global_load_dwordx4 v[12:15], v[68:69], off sc0 sc1 nt
	global_load_dwordx4 v[16:19], v[70:71], off sc0 sc1 nt
	s_waitcnt lgkmcnt(0)
	v_add_u32_e32 v171, 1, v171
	ds_write_b32 v169, v171
	ds_write_b64 v1, v[22:23]
	s_waitcnt vmcnt(14)
	v_cvt_pk_f16_f32 v21, v26, v27
	v_cvt_pk_f16_f32 v20, v24, v25
	v_add_u32_e32 v1, 0x12800, v0
	s_lshl_b32 s0, s0, 2
	ds_write_b64 v1, v[20:21]
	s_waitcnt vmcnt(13)
	v_cvt_pk_f16_f32 v20, v28, v29
	v_lshl_add_u64 v[28:29], v[2:3], 0, s[0:1]
	v_cvt_pk_f16_f32 v21, v30, v31
	v_add_co_u32_e32 v30, vcc, s3, v28
	v_add_u32_e32 v1, 0x13000, v0
	s_nop 0
	v_addc_co_u32_e32 v31, vcc, 0, v29, vcc
	v_add_co_u32_e32 v68, vcc, s4, v28
	ds_write_b64 v1, v[20:21]
	s_waitcnt vmcnt(12)
	v_cvt_pk_f16_f32 v21, v34, v35
	v_cvt_pk_f16_f32 v20, v32, v33
	v_add_u32_e32 v1, 0x13800, v0
	v_addc_co_u32_e32 v69, vcc, 0, v29, vcc
	s_add_i32 s0, s2, 0x380
	ds_write_b64 v1, v[20:21]
	v_add_co_u32_e32 v70, vcc, s5, v28
	s_waitcnt vmcnt(11)
	v_cvt_pk_f16_f32 v39, v38, v39
	v_cvt_pk_f16_f32 v38, v36, v37
	v_add_u32_e32 v1, 0x14000, v0
	s_and_b32 s0, s0, 0x3c0
	global_load_dwordx4 v[20:23], v[28:29], off sc0 sc1 nt
	global_load_dwordx4 v[24:27], v[30:31], off sc0 sc1 nt
	v_addc_co_u32_e32 v71, vcc, 0, v29, vcc
	global_load_dwordx4 v[28:31], v[68:69], off sc0 sc1 nt
	global_load_dwordx4 v[32:35], v[70:71], off sc0 sc1 nt
	s_waitcnt lgkmcnt(0)
	v_add_u32_e32 v171, 1, v171
	ds_write_b32 v169, v171
	ds_write_b64 v1, v[38:39]
	s_waitcnt vmcnt(14)
	v_cvt_pk_f16_f32 v37, v42, v43
	v_cvt_pk_f16_f32 v36, v40, v41
	v_add_u32_e32 v1, 0x14800, v0
	s_lshl_b32 s0, s0, 2
	ds_write_b64 v1, v[36:37]
	s_waitcnt vmcnt(13)
	v_cvt_pk_f16_f32 v36, v44, v45
	v_lshl_add_u64 v[44:45], v[2:3], 0, s[0:1]
	v_cvt_pk_f16_f32 v37, v46, v47
	v_add_co_u32_e32 v46, vcc, s3, v44
	s_addk_i32 s2, 0x3c0
	s_nop 0
	v_addc_co_u32_e32 v47, vcc, 0, v45, vcc
	v_add_co_u32_e32 v68, vcc, s4, v44
	v_add_u32_e32 v1, 0x15000, v0
	s_nop 0
	v_addc_co_u32_e32 v69, vcc, 0, v45, vcc
	s_and_b32 s0, s2, 0x3c0
	ds_write_b64 v1, v[36:37]
	s_waitcnt vmcnt(12)
	v_cvt_pk_f16_f32 v37, v50, v51
	v_cvt_pk_f16_f32 v36, v48, v49
	v_add_u32_e32 v1, 0x15800, v0
	v_add_co_u32_e32 v70, vcc, s5, v44
	s_lshl_b32 s0, s0, 2
	ds_write_b64 v1, v[36:37]
	v_addc_co_u32_e32 v71, vcc, 0, v45, vcc
	v_lshl_add_u64 v[2:3], v[2:3], 0, s[0:1]
	global_load_dwordx4 v[36:39], v[44:45], off sc0 sc1 nt
	global_load_dwordx4 v[40:43], v[46:47], off sc0 sc1 nt
	s_waitcnt vmcnt(13)
	v_cvt_pk_f16_f32 v55, v54, v55
	v_cvt_pk_f16_f32 v54, v52, v53
	s_waitcnt vmcnt(12)
	v_cvt_pk_f16_f32 v52, v56, v57
	v_add_co_u32_e32 v56, vcc, s3, v2
	v_add_u32_e32 v1, 0x16000, v0
	s_nop 0
	v_addc_co_u32_e32 v57, vcc, 0, v3, vcc
	global_load_dwordx4 v[44:47], v[68:69], off sc0 sc1 nt
	global_load_dwordx4 v[48:51], v[70:71], off sc0 sc1 nt
	s_waitcnt lgkmcnt(0)
	v_add_u32_e32 v171, 1, v171
	ds_write_b32 v169, v171
	ds_write_b64 v1, v[54:55]
	v_cvt_pk_f16_f32 v53, v58, v59
	v_add_u32_e32 v1, 0x16800, v0
	v_add_co_u32_e32 v68, vcc, s4, v2
	ds_write_b64 v1, v[52:53]
	global_load_dwordx4 v[52:55], v[2:3], off sc0 sc1 nt
	v_addc_co_u32_e32 v69, vcc, 0, v3, vcc
	global_load_dwordx4 v[56:59], v[56:57], off sc0 sc1 nt
	v_add_co_u32_e32 v2, vcc, s5, v2
	global_load_dwordx4 v[68:71], v[68:69], off sc0 sc1 nt
	s_nop 0
	v_addc_co_u32_e32 v3, vcc, 0, v3, vcc
	global_load_dwordx4 v[72:75], v[2:3], off sc0 sc1 nt
	s_waitcnt vmcnt(17)
	v_cvt_pk_f16_f32 v63, v62, v63
	v_cvt_pk_f16_f32 v62, v60, v61
	v_add_u32_e32 v1, 0x17000, v0
	ds_write_b64 v1, v[62:63]
	s_waitcnt vmcnt(16)
	v_cvt_pk_f16_f32 v3, v66, v67
	v_cvt_pk_f16_f32 v2, v64, v65
	v_add_u32_e32 v1, 0x17800, v0
	ds_write_b64 v1, v[2:3]
	s_waitcnt vmcnt(15)
	v_cvt_pk_f16_f32 v3, v6, v7
	v_cvt_pk_f16_f32 v2, v4, v5
	v_add_u32_e32 v1, 0x18000, v0
	s_waitcnt lgkmcnt(0)
	v_add_u32_e32 v171, 1, v171
	ds_write_b32 v169, v171
	ds_write_b64 v1, v[2:3]
	s_waitcnt vmcnt(14)
	v_cvt_pk_f16_f32 v3, v10, v11
	v_cvt_pk_f16_f32 v2, v8, v9
	v_add_u32_e32 v1, 0x18800, v0
	ds_write_b64 v1, v[2:3]
	s_waitcnt vmcnt(13)
	v_cvt_pk_f16_f32 v3, v14, v15
	v_cvt_pk_f16_f32 v2, v12, v13
	v_add_u32_e32 v1, 0x19000, v0
	ds_write_b64 v1, v[2:3]
	s_waitcnt vmcnt(12)
	v_cvt_pk_f16_f32 v3, v18, v19
	v_cvt_pk_f16_f32 v2, v16, v17
	v_add_u32_e32 v1, 0x19800, v0
	ds_write_b64 v1, v[2:3]
	s_waitcnt vmcnt(11)
	v_cvt_pk_f16_f32 v3, v22, v23
	v_cvt_pk_f16_f32 v2, v20, v21
	v_add_u32_e32 v1, 0x1a000, v0
	s_waitcnt lgkmcnt(0)
	v_add_u32_e32 v171, 1, v171
	ds_write_b32 v169, v171
	ds_write_b64 v1, v[2:3]
	s_waitcnt vmcnt(10)
	v_cvt_pk_f16_f32 v3, v26, v27
	v_cvt_pk_f16_f32 v2, v24, v25
	v_add_u32_e32 v1, 0x1a800, v0
	ds_write_b64 v1, v[2:3]
	s_waitcnt vmcnt(9)
	v_cvt_pk_f16_f32 v3, v30, v31
	v_cvt_pk_f16_f32 v2, v28, v29
	v_add_u32_e32 v1, 0x1b000, v0
	ds_write_b64 v1, v[2:3]
	s_waitcnt vmcnt(8)
	v_cvt_pk_f16_f32 v3, v34, v35
	v_cvt_pk_f16_f32 v2, v32, v33
	v_add_u32_e32 v1, 0x1b800, v0
	ds_write_b64 v1, v[2:3]
	v_add_u32_e32 v1, 0x1c000, v0
	s_waitcnt lgkmcnt(0)
	v_add_u32_e32 v171, 1, v171
	ds_write_b32 v169, v171
	s_waitcnt vmcnt(7)
	v_cvt_pk_f16_f32 v3, v38, v39
	v_cvt_pk_f16_f32 v2, v36, v37
	ds_write_b64 v1, v[2:3]
	s_waitcnt vmcnt(6)
	v_cvt_pk_f16_f32 v3, v42, v43
	v_cvt_pk_f16_f32 v2, v40, v41
	v_add_u32_e32 v1, 0x1c800, v0
	ds_write_b64 v1, v[2:3]
	v_add_u32_e32 v1, 0x1d000, v0
	s_waitcnt vmcnt(5)
	v_cvt_pk_f16_f32 v3, v46, v47
	v_cvt_pk_f16_f32 v2, v44, v45
	ds_write_b64 v1, v[2:3]
	s_waitcnt vmcnt(4)
	v_cvt_pk_f16_f32 v3, v50, v51
	v_cvt_pk_f16_f32 v2, v48, v49
	v_add_u32_e32 v1, 0x1d800, v0
	ds_write_b64 v1, v[2:3]
	v_add_u32_e32 v1, 0x1e000, v0
	s_waitcnt lgkmcnt(0)
	v_add_u32_e32 v171, 1, v171
	ds_write_b32 v169, v171
	s_waitcnt vmcnt(3)
	v_cvt_pk_f16_f32 v3, v54, v55
	v_cvt_pk_f16_f32 v2, v52, v53
	ds_write_b64 v1, v[2:3]
	s_waitcnt vmcnt(2)
	v_cvt_pk_f16_f32 v3, v58, v59
	v_cvt_pk_f16_f32 v2, v56, v57
	v_add_u32_e32 v1, 0x1e800, v0
	ds_write_b64 v1, v[2:3]
	s_waitcnt vmcnt(1)
	v_cvt_pk_f16_f32 v3, v70, v71
	v_cvt_pk_f16_f32 v2, v68, v69
	v_add_u32_e32 v1, 0x1f000, v0
	ds_write_b64 v1, v[2:3]
	s_waitcnt vmcnt(0)
	v_cvt_pk_f16_f32 v3, v74, v75
	v_cvt_pk_f16_f32 v2, v72, v73
	v_add_u32_e32 v0, 0x1f800, v0
	ds_write_b64 v0, v[2:3]
	s_waitcnt lgkmcnt(0)
	v_add_u32_e32 v171, 1, v171
	ds_write_b32 v169, v171
	s_waitcnt lgkmcnt(0)
	s_endpgm
